# att4_hoist_lds_staging_writes
# speedup vs baseline: 1.0062x; 1.0062x over previous
.LBB0_825:
	ds_read_b64_tr_b16 v[190:191], v234 offset:0x600
	ds_read_b64_tr_b16 v[192:193], v234 offset:0xe00
	ds_read_b64_tr_b16 v[236:237], v234 offset:0x1600
	ds_read_b64_tr_b16 v[238:239], v234 offset:0x1e00
	ds_read_b64_tr_b16 v[240:241], v234 offset:0x2600
	ds_read_b64_tr_b16 v[242:243], v234 offset:0x2e00
	ds_read_b64_tr_b16 v[244:245], v234 offset:0x3600
	ds_read_b64_tr_b16 v[246:247], v234 offset:0x3e00
	s_waitcnt lgkmcnt(8)
	v_mfma_f32_32x32x16_bf16 v[32:47], v[96:99], v[124:127], v[32:47]
	v_exp_f32_e32 v128, v128
	v_exp_f32_e32 v129, v129
	v_exp_f32_e32 v130, v130
	v_exp_f32_e32 v131, v131
	v_exp_f32_e32 v132, v132
	v_exp_f32_e32 v133, v133
	v_exp_f32_e32 v134, v134
	v_mfma_f32_32x32x16_bf16 v[32:47], v[120:123], v[116:119], v[32:47]
	v_exp_f32_e32 v135, v135
	v_exp_f32_e32 v136, v136
	v_exp_f32_e32 v137, v137
	v_exp_f32_e32 v138, v138
	v_exp_f32_e32 v139, v139
	v_mfma_f32_32x32x16_bf16 v[32:47], v[104:107], v[112:115], v[32:47]
	v_mfma_f32_32x32x16_bf16 v[32:47], v[100:103], v[108:111], v[32:47]
	s_waitcnt lgkmcnt(0)
	s_lshl_b32 s2, s41, 14
	s_add_i32 s2, s2, 0
	v_add_u32_e32 v64, s2, v218
	s_lshl_b32 s3, s41, 13
	s_waitcnt vmcnt(2)
	ds_write_b128 v64, v[178:181]
	v_add_u32_e32 v64, s2, v219
	s_sub_i32 s2, s2, s3
	s_waitcnt vmcnt(1)
	ds_write_b128 v64, v[182:185]
	v_add_u32_e32 v64, s2, v220
	s_waitcnt vmcnt(0)
	ds_write_b128 v64, v[186:189] offset:49152
	v_mfma_f32_32x32x16_bf16 v[16:31], v[96:99], v[190:193], v[16:31]
	v_exp_f32_e32 v140, v140
	v_exp_f32_e32 v141, v141
	v_exp_f32_e32 v142, v142
	v_exp_f32_e32 v143, v143
	v_exp_f32_e32 v144, v144
	v_exp_f32_e32 v145, v145
	v_exp_f32_e32 v146, v146
	v_mfma_f32_32x32x16_bf16 v[16:31], v[120:123], v[236:239], v[16:31]
	v_exp_f32_e32 v147, v147
	v_exp_f32_e32 v148, v148
	v_exp_f32_e32 v149, v149
	v_exp_f32_e32 v150, v150
	v_exp_f32_e32 v151, v151
	v_cmp_gt_f32_e32 vcc, 1.0, v233
	v_mfma_f32_32x32x16_bf16 v[16:31], v[104:107], v[240:243], v[16:31]
	v_mfma_f32_32x32x16_bf16 v[16:31], v[100:103], v[244:247], v[16:31]
	s_cbranch_vccz .LBB0_829
	s_and_saveexec_b64 s[12:13], s[0:1]
	ds_write_b32 v214, v233 offset:128
	s_or_b64 exec, exec, s[12:13]
	s_waitcnt lgkmcnt(0)
	v_add_u32_e32 v108, v213, v160
	ds_read_b128 v[96:99], v108 offset:224
	ds_read_b128 v[100:103], v108 offset:192
	ds_read_b128 v[104:107], v108 offset:160
	ds_read_b128 v[108:111], v108 offset:128
	s_waitcnt lgkmcnt(3)
	v_pk_mul_f32 v[12:13], v[12:13], v[96:97]
	s_waitcnt lgkmcnt(2)
	v_pk_mul_f32 v[8:9], v[8:9], v[100:101]
	s_waitcnt lgkmcnt(1)
	v_pk_mul_f32 v[4:5], v[4:5], v[104:105]
	v_pk_mul_f32 v[14:15], v[14:15], v[98:99]
	v_pk_mul_f32 v[10:11], v[10:11], v[102:103]
	v_pk_mul_f32 v[6:7], v[6:7], v[106:107]
	s_waitcnt lgkmcnt(0)
	v_pk_mul_f32 v[2:3], v[2:3], v[110:111]
	v_pk_mul_f32 v[0:1], v[0:1], v[108:109]
	v_pk_mul_f32 v[60:61], v[60:61], v[96:97]
	v_pk_mul_f32 v[56:57], v[56:57], v[100:101]
	v_pk_mul_f32 v[52:53], v[52:53], v[104:105]
	v_pk_mul_f32 v[62:63], v[62:63], v[98:99]
	v_pk_mul_f32 v[58:59], v[58:59], v[102:103]
	v_pk_mul_f32 v[54:55], v[54:55], v[106:107]
	v_pk_mul_f32 v[50:51], v[50:51], v[110:111]
	v_pk_mul_f32 v[48:49], v[48:49], v[108:109]
	v_pk_mul_f32 v[44:45], v[44:45], v[96:97]
	v_pk_mul_f32 v[40:41], v[40:41], v[100:101]
	v_pk_mul_f32 v[36:37], v[36:37], v[104:105]
	v_pk_mul_f32 v[46:47], v[46:47], v[98:99]
	v_pk_mul_f32 v[42:43], v[42:43], v[102:103]
	v_pk_mul_f32 v[38:39], v[38:39], v[106:107]
	v_pk_mul_f32 v[34:35], v[34:35], v[110:111]
	v_pk_mul_f32 v[32:33], v[32:33], v[108:109]
	v_pk_mul_f32 v[28:29], v[28:29], v[96:97]
	v_pk_mul_f32 v[24:25], v[24:25], v[100:101]
	v_pk_mul_f32 v[20:21], v[20:21], v[104:105]
	v_pk_mul_f32 v[30:31], v[30:31], v[98:99]
	v_pk_mul_f32 v[26:27], v[26:27], v[102:103]
	v_pk_mul_f32 v[22:23], v[22:23], v[106:107]
	v_pk_mul_f32 v[18:19], v[18:19], v[110:111]
	v_pk_mul_f32 v[16:17], v[16:17], v[108:109]

.LBB0_830:
	ds_read_b64_tr_b16 v[190:191], v205 offset:0x600
	ds_read_b64_tr_b16 v[192:193], v205 offset:0xe00
	ds_read_b64_tr_b16 v[234:235], v205 offset:0x1600
	ds_read_b64_tr_b16 v[236:237], v205 offset:0x1e00
	ds_read_b64_tr_b16 v[238:239], v205 offset:0x2600
	ds_read_b64_tr_b16 v[240:241], v205 offset:0x2e00
	ds_read_b64_tr_b16 v[242:243], v205 offset:0x3600
	ds_read_b64_tr_b16 v[244:245], v205 offset:0x3e00
	s_add_i32 s2, s41, 1
	s_waitcnt lgkmcnt(8)
	s_cmp_lg_u32 s41, 2
	s_cselect_b32 s42, s2, 0
	v_mfma_f32_32x32x16_bf16 v[32:47], v[152:155], v[156:159], v[32:47]
	v_exp_f32_e32 v96, v96
	v_exp_f32_e32 v97, v97
	v_exp_f32_e32 v98, v98
	v_exp_f32_e32 v99, v99
	v_exp_f32_e32 v100, v100
	v_exp_f32_e32 v101, v101
	v_exp_f32_e32 v102, v102
	v_mfma_f32_32x32x16_bf16 v[32:47], v[136:139], v[148:151], v[32:47]
	v_exp_f32_e32 v103, v103
	v_exp_f32_e32 v104, v104
	v_exp_f32_e32 v105, v105
	v_exp_f32_e32 v106, v106
	v_exp_f32_e32 v107, v107
	v_mfma_f32_32x32x16_bf16 v[32:47], v[132:135], v[144:147], v[32:47]
	v_mfma_f32_32x32x16_bf16 v[32:47], v[128:131], v[140:143], v[32:47]
	s_waitcnt lgkmcnt(0)
	s_lshl_b32 s2, s42, 14
	s_add_i32 s2, s2, 0
	v_add_u32_e32 v64, s2, v218
	s_waitcnt vmcnt(2)
	ds_write_b128 v64, v[178:181]
	v_add_u32_e32 v64, s2, v219
	s_waitcnt vmcnt(1)
	ds_write_b128 v64, v[182:185]
	v_lshl_add_u32 v64, s42, 13, v221
	s_waitcnt vmcnt(0)
	ds_write_b128 v64, v[186:189] offset:49152
	v_mfma_f32_32x32x16_bf16 v[16:31], v[152:155], v[190:193], v[16:31]
	v_exp_f32_e32 v108, v108
	v_exp_f32_e32 v109, v109
	v_exp_f32_e32 v110, v110
	v_exp_f32_e32 v111, v111
	v_exp_f32_e32 v112, v112
	v_exp_f32_e32 v113, v113
	v_exp_f32_e32 v114, v114
	v_mfma_f32_32x32x16_bf16 v[16:31], v[136:139], v[234:237], v[16:31]
	v_exp_f32_e32 v115, v115
	v_exp_f32_e32 v116, v116
	v_exp_f32_e32 v117, v117
	v_exp_f32_e32 v118, v118
	v_exp_f32_e32 v119, v119
	v_cmp_gt_f32_e32 vcc, 1.0, v202
	v_mfma_f32_32x32x16_bf16 v[16:31], v[132:135], v[238:241], v[16:31]
	v_mfma_f32_32x32x16_bf16 v[16:31], v[128:131], v[242:245], v[16:31]
	s_cbranch_vccz .LBB0_834
	s_and_saveexec_b64 s[12:13], s[0:1]
	ds_write_b32 v214, v202 offset:128
	s_or_b64 exec, exec, s[12:13]
	s_waitcnt lgkmcnt(0)
	v_add_u32_e32 v140, v213, v160
	ds_read_b128 v[128:131], v140 offset:224
	ds_read_b128 v[132:135], v140 offset:192
	ds_read_b128 v[136:139], v140 offset:160
	ds_read_b128 v[140:143], v140 offset:128
	s_waitcnt lgkmcnt(3)
	v_pk_mul_f32 v[12:13], v[12:13], v[128:129]
	s_waitcnt lgkmcnt(2)
	v_pk_mul_f32 v[8:9], v[8:9], v[132:133]
	s_waitcnt lgkmcnt(1)
	v_pk_mul_f32 v[4:5], v[4:5], v[136:137]
	v_pk_mul_f32 v[14:15], v[14:15], v[130:131]
	v_pk_mul_f32 v[10:11], v[10:11], v[134:135]
	v_pk_mul_f32 v[6:7], v[6:7], v[138:139]
	s_waitcnt lgkmcnt(0)
	v_pk_mul_f32 v[2:3], v[2:3], v[142:143]
	v_pk_mul_f32 v[0:1], v[0:1], v[140:141]
	v_pk_mul_f32 v[60:61], v[60:61], v[128:129]
	v_pk_mul_f32 v[56:57], v[56:57], v[132:133]
	v_pk_mul_f32 v[52:53], v[52:53], v[136:137]
	v_pk_mul_f32 v[62:63], v[62:63], v[130:131]
	v_pk_mul_f32 v[58:59], v[58:59], v[134:135]
	v_pk_mul_f32 v[54:55], v[54:55], v[138:139]
	v_pk_mul_f32 v[50:51], v[50:51], v[142:143]
	v_pk_mul_f32 v[48:49], v[48:49], v[140:141]
	v_pk_mul_f32 v[44:45], v[44:45], v[128:129]
	v_pk_mul_f32 v[40:41], v[40:41], v[132:133]
	v_pk_mul_f32 v[36:37], v[36:37], v[136:137]
	v_pk_mul_f32 v[46:47], v[46:47], v[130:131]
	v_pk_mul_f32 v[42:43], v[42:43], v[134:135]
	v_pk_mul_f32 v[38:39], v[38:39], v[138:139]
	v_pk_mul_f32 v[34:35], v[34:35], v[142:143]
	v_pk_mul_f32 v[32:33], v[32:33], v[140:141]
	v_pk_mul_f32 v[28:29], v[28:29], v[128:129]
	v_pk_mul_f32 v[24:25], v[24:25], v[132:133]
	v_pk_mul_f32 v[20:21], v[20:21], v[136:137]
	v_pk_mul_f32 v[30:31], v[30:31], v[130:131]
	v_pk_mul_f32 v[26:27], v[26:27], v[134:135]
	v_pk_mul_f32 v[22:23], v[22:23], v[138:139]
	v_pk_mul_f32 v[18:19], v[18:19], v[142:143]
	v_pk_mul_f32 v[16:17], v[16:17], v[140:141]

.LBB0_848:
	ds_read_b64_tr_b16 v[190:191], v238 offset:0x600
	ds_read_b64_tr_b16 v[192:193], v238 offset:0xe00
	ds_read_b64_tr_b16 v[208:209], v238 offset:0x1600
	ds_read_b64_tr_b16 v[210:211], v238 offset:0x1e00
	ds_read_b64_tr_b16 v[240:241], v238 offset:0x2600
	ds_read_b64_tr_b16 v[242:243], v238 offset:0x2e00
	ds_read_b64_tr_b16 v[244:245], v238 offset:0x3600
	ds_read_b64_tr_b16 v[246:247], v238 offset:0x3e00
	s_waitcnt lgkmcnt(8)
	v_mfma_f32_32x32x16_bf16 v[32:47], v[96:99], v[124:127], v[32:47]
	v_exp_f32_e32 v128, v128
	v_exp_f32_e32 v129, v129
	v_exp_f32_e32 v130, v130
	v_exp_f32_e32 v131, v131
	v_exp_f32_e32 v132, v132
	v_exp_f32_e32 v133, v133
	v_exp_f32_e32 v134, v134
	v_mfma_f32_32x32x16_bf16 v[32:47], v[120:123], v[116:119], v[32:47]
	v_exp_f32_e32 v135, v135
	v_exp_f32_e32 v136, v136
	v_exp_f32_e32 v137, v137
	v_exp_f32_e32 v138, v138
	v_exp_f32_e32 v139, v139
	v_mfma_f32_32x32x16_bf16 v[32:47], v[104:107], v[112:115], v[32:47]
	v_mfma_f32_32x32x16_bf16 v[32:47], v[100:103], v[108:111], v[32:47]
	s_waitcnt lgkmcnt(0)
	s_lshl_b32 s2, s29, 14
	s_add_i32 s2, s2, 0
	v_add_u32_e32 v64, s2, v222
	s_lshl_b32 s3, s29, 13
	s_waitcnt vmcnt(2)
	ds_write_b128 v64, v[178:181]
	v_add_u32_e32 v64, s2, v223
	s_sub_i32 s2, s2, s3
	s_waitcnt vmcnt(1)
	ds_write_b128 v64, v[182:185]
	v_add_u32_e32 v64, s2, v224
	s_waitcnt vmcnt(0)
	ds_write_b128 v64, v[186:189] offset:49152
	v_mfma_f32_32x32x16_bf16 v[16:31], v[96:99], v[190:193], v[16:31]
	v_exp_f32_e32 v140, v140
	v_exp_f32_e32 v141, v141
	v_exp_f32_e32 v142, v142
	v_exp_f32_e32 v143, v143
	v_exp_f32_e32 v144, v144
	v_exp_f32_e32 v145, v145
	v_exp_f32_e32 v146, v146
	v_mfma_f32_32x32x16_bf16 v[16:31], v[120:123], v[208:211], v[16:31]
	v_exp_f32_e32 v147, v147
	v_exp_f32_e32 v148, v148
	v_exp_f32_e32 v149, v149
	v_exp_f32_e32 v150, v150
	v_exp_f32_e32 v151, v151
	v_cmp_gt_f32_e32 vcc, 1.0, v237
	v_mfma_f32_32x32x16_bf16 v[16:31], v[104:107], v[240:243], v[16:31]
	v_mfma_f32_32x32x16_bf16 v[16:31], v[100:103], v[244:247], v[16:31]
	s_cbranch_vccz .LBB0_852
	s_and_saveexec_b64 s[10:11], s[0:1]
	ds_write_b32 v218, v237 offset:128
	s_or_b64 exec, exec, s[10:11]
	s_waitcnt lgkmcnt(0)
	v_add_u32_e32 v108, v217, v160
	ds_read_b128 v[96:99], v108 offset:224
	ds_read_b128 v[100:103], v108 offset:192
	ds_read_b128 v[104:107], v108 offset:160
	ds_read_b128 v[108:111], v108 offset:128
	s_waitcnt lgkmcnt(3)
	v_pk_mul_f32 v[12:13], v[12:13], v[96:97]
	s_waitcnt lgkmcnt(2)
	v_pk_mul_f32 v[8:9], v[8:9], v[100:101]
	s_waitcnt lgkmcnt(1)
	v_pk_mul_f32 v[4:5], v[4:5], v[104:105]
	v_pk_mul_f32 v[14:15], v[14:15], v[98:99]
	v_pk_mul_f32 v[10:11], v[10:11], v[102:103]
	v_pk_mul_f32 v[6:7], v[6:7], v[106:107]
	s_waitcnt lgkmcnt(0)
	v_pk_mul_f32 v[2:3], v[2:3], v[110:111]
	v_pk_mul_f32 v[0:1], v[0:1], v[108:109]
	v_pk_mul_f32 v[60:61], v[60:61], v[96:97]
	v_pk_mul_f32 v[56:57], v[56:57], v[100:101]
	v_pk_mul_f32 v[52:53], v[52:53], v[104:105]
	v_pk_mul_f32 v[62:63], v[62:63], v[98:99]
	v_pk_mul_f32 v[58:59], v[58:59], v[102:103]
	v_pk_mul_f32 v[54:55], v[54:55], v[106:107]
	v_pk_mul_f32 v[50:51], v[50:51], v[110:111]
	v_pk_mul_f32 v[48:49], v[48:49], v[108:109]
	v_pk_mul_f32 v[44:45], v[44:45], v[96:97]
	v_pk_mul_f32 v[40:41], v[40:41], v[100:101]
	v_pk_mul_f32 v[36:37], v[36:37], v[104:105]
	v_pk_mul_f32 v[46:47], v[46:47], v[98:99]
	v_pk_mul_f32 v[42:43], v[42:43], v[102:103]
	v_pk_mul_f32 v[38:39], v[38:39], v[106:107]
	v_pk_mul_f32 v[34:35], v[34:35], v[110:111]
	v_pk_mul_f32 v[32:33], v[32:33], v[108:109]
	v_pk_mul_f32 v[28:29], v[28:29], v[96:97]
	v_pk_mul_f32 v[24:25], v[24:25], v[100:101]
	v_pk_mul_f32 v[20:21], v[20:21], v[104:105]
	v_pk_mul_f32 v[30:31], v[30:31], v[98:99]
	v_pk_mul_f32 v[26:27], v[26:27], v[102:103]
	v_pk_mul_f32 v[22:23], v[22:23], v[106:107]
	v_pk_mul_f32 v[18:19], v[18:19], v[110:111]
	v_pk_mul_f32 v[16:17], v[16:17], v[108:109]

.LBB0_853:
	ds_read_b64_tr_b16 v[190:191], v205 offset:0x600
	ds_read_b64_tr_b16 v[192:193], v205 offset:0xe00
	ds_read_b64_tr_b16 v[208:209], v205 offset:0x1600
	ds_read_b64_tr_b16 v[210:211], v205 offset:0x1e00
	ds_read_b64_tr_b16 v[238:239], v205 offset:0x2600
	ds_read_b64_tr_b16 v[240:241], v205 offset:0x2e00
	ds_read_b64_tr_b16 v[242:243], v205 offset:0x3600
	ds_read_b64_tr_b16 v[244:245], v205 offset:0x3e00
	s_add_i32 s2, s29, 1
	s_waitcnt lgkmcnt(8)
	s_cmp_lg_u32 s29, 2
	s_cselect_b32 s30, s2, 0
	v_mfma_f32_32x32x16_bf16 v[32:47], v[152:155], v[156:159], v[32:47]
	v_exp_f32_e32 v96, v96
	v_exp_f32_e32 v97, v97
	v_exp_f32_e32 v98, v98
	v_exp_f32_e32 v99, v99
	v_exp_f32_e32 v100, v100
	v_exp_f32_e32 v101, v101
	v_exp_f32_e32 v102, v102
	v_mfma_f32_32x32x16_bf16 v[32:47], v[136:139], v[148:151], v[32:47]
	v_exp_f32_e32 v103, v103
	v_exp_f32_e32 v104, v104
	v_exp_f32_e32 v105, v105
	v_exp_f32_e32 v106, v106
	v_exp_f32_e32 v107, v107
	v_mfma_f32_32x32x16_bf16 v[32:47], v[132:135], v[144:147], v[32:47]
	v_mfma_f32_32x32x16_bf16 v[32:47], v[128:131], v[140:143], v[32:47]
	s_waitcnt lgkmcnt(0)
	s_lshl_b32 s2, s30, 14
	s_add_i32 s2, s2, 0
	v_add_u32_e32 v64, s2, v222
	s_waitcnt vmcnt(2)
	ds_write_b128 v64, v[178:181]
	v_add_u32_e32 v64, s2, v223
	s_waitcnt vmcnt(1)
	ds_write_b128 v64, v[182:185]
	v_lshl_add_u32 v64, s30, 13, v225
	s_waitcnt vmcnt(0)
	ds_write_b128 v64, v[186:189] offset:49152
	v_mfma_f32_32x32x16_bf16 v[16:31], v[152:155], v[190:193], v[16:31]
	v_exp_f32_e32 v108, v108
	v_exp_f32_e32 v109, v109
	v_exp_f32_e32 v110, v110
	v_exp_f32_e32 v111, v111
	v_exp_f32_e32 v112, v112
	v_exp_f32_e32 v113, v113
	v_exp_f32_e32 v114, v114
	v_mfma_f32_32x32x16_bf16 v[16:31], v[136:139], v[208:211], v[16:31]
	v_exp_f32_e32 v115, v115
	v_exp_f32_e32 v116, v116
	v_exp_f32_e32 v117, v117
	v_exp_f32_e32 v118, v118
	v_exp_f32_e32 v119, v119
	v_cmp_gt_f32_e32 vcc, 1.0, v202
	v_mfma_f32_32x32x16_bf16 v[16:31], v[132:135], v[238:241], v[16:31]
	v_mfma_f32_32x32x16_bf16 v[16:31], v[128:131], v[242:245], v[16:31]
	s_cbranch_vccz .LBB0_857
	s_and_saveexec_b64 s[10:11], s[0:1]
	ds_write_b32 v218, v202 offset:128
	s_or_b64 exec, exec, s[10:11]
	s_waitcnt lgkmcnt(0)
	v_add_u32_e32 v140, v217, v160
	ds_read_b128 v[128:131], v140 offset:224
	ds_read_b128 v[132:135], v140 offset:192
	ds_read_b128 v[136:139], v140 offset:160
	ds_read_b128 v[140:143], v140 offset:128
	s_waitcnt lgkmcnt(3)
	v_pk_mul_f32 v[12:13], v[12:13], v[128:129]
	s_waitcnt lgkmcnt(2)
	v_pk_mul_f32 v[8:9], v[8:9], v[132:133]
	s_waitcnt lgkmcnt(1)
	v_pk_mul_f32 v[4:5], v[4:5], v[136:137]
	v_pk_mul_f32 v[14:15], v[14:15], v[130:131]
	v_pk_mul_f32 v[10:11], v[10:11], v[134:135]
	v_pk_mul_f32 v[6:7], v[6:7], v[138:139]
	s_waitcnt lgkmcnt(0)
	v_pk_mul_f32 v[2:3], v[2:3], v[142:143]
	v_pk_mul_f32 v[0:1], v[0:1], v[140:141]
	v_pk_mul_f32 v[60:61], v[60:61], v[128:129]
	v_pk_mul_f32 v[56:57], v[56:57], v[132:133]
	v_pk_mul_f32 v[52:53], v[52:53], v[136:137]
	v_pk_mul_f32 v[62:63], v[62:63], v[130:131]
	v_pk_mul_f32 v[58:59], v[58:59], v[134:135]
	v_pk_mul_f32 v[54:55], v[54:55], v[138:139]
	v_pk_mul_f32 v[50:51], v[50:51], v[142:143]
	v_pk_mul_f32 v[48:49], v[48:49], v[140:141]
	v_pk_mul_f32 v[44:45], v[44:45], v[128:129]
	v_pk_mul_f32 v[40:41], v[40:41], v[132:133]
	v_pk_mul_f32 v[36:37], v[36:37], v[136:137]
	v_pk_mul_f32 v[46:47], v[46:47], v[130:131]
	v_pk_mul_f32 v[42:43], v[42:43], v[134:135]
	v_pk_mul_f32 v[38:39], v[38:39], v[138:139]
	v_pk_mul_f32 v[34:35], v[34:35], v[142:143]
	v_pk_mul_f32 v[32:33], v[32:33], v[140:141]
	v_pk_mul_f32 v[28:29], v[28:29], v[128:129]
	v_pk_mul_f32 v[24:25], v[24:25], v[132:133]
	v_pk_mul_f32 v[20:21], v[20:21], v[136:137]
	v_pk_mul_f32 v[30:31], v[30:31], v[130:131]
	v_pk_mul_f32 v[26:27], v[26:27], v[134:135]
	v_pk_mul_f32 v[22:23], v[22:23], v[138:139]
	v_pk_mul_f32 v[18:19], v[18:19], v[142:143]
	v_pk_mul_f32 v[16:17], v[16:17], v[140:141]
